# p1: gather one pass ahead + the next pass's row prefetch no longer forced mid-pass (modulation block retires its loads, mid-pass full wait removed, prefetched pass skips the gather wait)
# baseline (speedup 1.0000x reference)
; __device__ __forceinline__ void p1_norm1(const Frame& F, int layer, int probe_rerun) {
;     ...
;         if (mR != cur_m) { cur_m = mR;
;             const float* sh = modl + mR * 6144; const float* sc = sh + 1024; const float* g2 = modp + mR * 6144 + 5 * 1024;
; #pragma unroll
;             for (int j = 0; j < 4; ++j) { const int k = 4 * (lane + 64 * j);
;                 if (!fin) { W1[j] = *(const f32x4*)(n1w + k) * (*(const f32x4*)(sc + k) + 1.f); S0[j] = *(const f32x4*)(sh + k); }
;                 if (layer > 0) G2[j] = *(const f32x4*)(g2 + k); } }
.LBB0_165:
	s_waitcnt vmcnt(7)
	v_pk_add_f32 v[116:117], v[116:117], 1.0 op_sel_hi:[1,0]
	v_pk_add_f32 v[76:77], v[76:77], 1.0 op_sel_hi:[1,0]
	s_waitcnt vmcnt(4)
	v_pk_add_f32 v[126:127], v[126:127], 1.0 op_sel_hi:[1,0]
	v_pk_add_f32 v[124:125], v[124:125], 1.0 op_sel_hi:[1,0]
	v_pk_add_f32 v[118:119], v[118:119], 1.0 op_sel_hi:[1,0]
	v_pk_mul_f32 v[68:69], v[68:69], v[116:117]
	v_pk_add_f32 v[78:79], v[78:79], 1.0 op_sel_hi:[1,0]
	v_pk_mul_f32 v[72:73], v[72:73], v[76:77]
	s_waitcnt vmcnt(0)
	v_pk_add_f32 v[76:77], v[122:123], 1.0 op_sel_hi:[1,0]
	v_pk_add_f32 v[116:117], v[120:121], 1.0 op_sel_hi:[1,0]
	v_pk_mul_f32 v[66:67], v[66:67], v[126:127]
	v_pk_mul_f32 v[64:65], v[64:65], v[124:125]
	v_pk_mul_f32 v[70:71], v[70:71], v[118:119]
	v_pk_mul_f32 v[74:75], v[74:75], v[78:79]
	v_pk_mul_f32 v[78:79], v[114:115], v[76:77]
	v_pk_mul_f32 v[76:77], v[112:113], v[116:117]
	s_mov_b32 s34, s7

; __device__ __forceinline__ float bflo(unsigned w) { return __uint_as_float(w << 16); }
; __device__ __forceinline__ float bfhi(unsigned w) { return __uint_as_float(w & 0xffff0000u); }
; __device__ __forceinline__ int shl_from_i(int v, int src_lane) { return __builtin_amdgcn_ds_bpermute(src_lane << 2, v); }
; __device__ __forceinline__ void p1_gather_consume(f32x4 (&va)[4], f32x4 (&vb)[4], u32x2 (&wa)[4][4], u32x2 (&wb)[4][4], unsigned maska, unsigned maskb, int inva, int invb,
;                                                   const bf16_t* Yp, const bf16_t* zrow, const f32x4 (&g2)[4], int lane) {
;     ...
;     for (;;) {
; #pragma unroll
;         for (int q = 0; q < 4; ++q)
; #pragma unroll
;             for (int j = 0; j < 4; ++j) { aa[j] += (f32x4){bflo(wa[q][j].x), bfhi(wa[q][j].x), bflo(wa[q][j].y), bfhi(wa[q][j].y)};
;                 ab[j] += (f32x4){bflo(wb[q][j].x), bfhi(wb[q][j].x), bflo(wb[q][j].y), bfhi(wb[q][j].y)}; }
;         if (!(maska | maskb)) break;
;         const bf16_t* ypa[4]; const bf16_t* ypb[4];
; #pragma unroll
;         for (int q = 0; q < 4; ++q) {
;             if (maska) { const int e = __builtin_ctz(maska); maska &= maska - 1; ypa[q] = Yp + (size_t)shl_from_i(inva, e) * D; } else ypa[q] = zrow;
;             if (maskb) { const int e = __builtin_ctz(maskb); maskb &= maskb - 1; ypb[q] = Yp + (size_t)shl_from_i(invb, e) * D; } else ypb[q] = zrow; }
; #pragma unroll
;         for (int q = 0; q < 4; ++q)
; #pragma unroll
;             for (int j = 0; j < 4; ++j) { wa[q][j] = *(const u32x2*)(ypa[q] + 4 * (lane + 64 * j)); wb[q][j] = *(const u32x2*)(ypb[q] + 4 * (lane + 64 * j)); }
.LBB0_185:
	v_lshl_add_u64 v[174:175], v[174:175], 0, v[112:113]
	global_load_dwordx2 v[226:227], v[174:175], off
	global_load_dwordx2 v[220:221], v[174:175], off offset:512
	global_load_dwordx2 v[216:217], v[174:175], off offset:1024
	global_load_dwordx2 v[210:211], v[174:175], off offset:1536
	v_lshl_add_u64 v[174:175], v[176:177], 0, v[112:113]
	v_lshl_add_u64 v[178:179], v[186:187], 0, v[112:113]
	v_lshl_add_u64 v[168:169], v[168:169], 0, v[112:113]
	global_load_dwordx2 v[206:207], v[174:175], off
	global_load_dwordx2 v[200:201], v[174:175], off offset:512
	global_load_dwordx2 v[194:195], v[174:175], off offset:1024
	global_load_dwordx2 v[190:191], v[174:175], off offset:1536
	global_load_dwordx2 v[186:187], v[178:179], off
	global_load_dwordx2 v[176:177], v[178:179], off offset:512
	s_nop 0
	global_load_dwordx2 v[174:175], v[178:179], off offset:1024
	global_load_dwordx2 v[232:233], v[168:169], off
	global_load_dwordx2 v[230:231], v[168:169], off offset:512
	global_load_dwordx2 v[228:229], v[168:169], off offset:1024
	global_load_dwordx2 v[224:225], v[168:169], off offset:1536
	v_lshl_add_u64 v[168:169], v[182:183], 0, v[112:113]
	global_load_dwordx2 v[222:223], v[168:169], off
	global_load_dwordx2 v[218:219], v[168:169], off offset:512
	global_load_dwordx2 v[214:215], v[168:169], off offset:1024
	global_load_dwordx2 v[204:205], v[168:169], off offset:1536
	s_nop 0
	global_load_dwordx2 v[168:169], v[178:179], off offset:1536
	v_lshl_add_u64 v[178:179], v[188:189], 0, v[112:113]
	global_load_dwordx2 v[202:203], v[178:179], off
	global_load_dwordx2 v[196:197], v[178:179], off offset:512
	global_load_dwordx2 v[188:189], v[178:179], off offset:1024
	global_load_dwordx2 v[182:183], v[178:179], off offset:1536
	s_waitcnt vmcnt(0) lgkmcnt(0)
.Lp1pf_wait:
	v_lshlrev_b32_e32 v178, 16, v212
	v_and_b32_e32 v179, 0xffff0000, v212
	v_pk_add_f32 v[166:167], v[166:167], v[178:179]
	v_lshlrev_b32_e32 v178, 16, v208
	v_and_b32_e32 v179, 0xffff0000, v208
	v_pk_add_f32 v[162:163], v[162:163], v[178:179]
	v_lshlrev_b32_e32 v178, 16, v198
	v_and_b32_e32 v179, 0xffff0000, v198
	v_pk_add_f32 v[158:159], v[158:159], v[178:179]
	v_lshlrev_b32_e32 v178, 16, v192
	v_and_b32_e32 v179, 0xffff0000, v192
	v_pk_add_f32 v[154:155], v[154:155], v[178:179]
	v_lshlrev_b32_e32 v178, 16, v184
	v_and_b32_e32 v179, 0xffff0000, v184
	v_pk_add_f32 v[146:147], v[146:147], v[178:179]
	v_lshlrev_b32_e32 v178, 16, v180
	v_and_b32_e32 v179, 0xffff0000, v180
	v_pk_add_f32 v[124:125], v[124:125], v[178:179]
	v_lshlrev_b32_e32 v178, 16, v172
	v_and_b32_e32 v179, 0xffff0000, v172
	v_lshlrev_b32_e32 v172, 16, v173
	v_and_b32_e32 v173, 0xffff0000, v173
	v_pk_add_f32 v[118:119], v[118:119], v[172:173]
	v_lshlrev_b32_e32 v172, 16, v170
	v_and_b32_e32 v173, 0xffff0000, v170
	v_lshlrev_b32_e32 v170, 16, v171
	v_and_b32_e32 v171, 0xffff0000, v171
	v_pk_add_f32 v[116:117], v[116:117], v[170:171]
	v_lshlrev_b32_e32 v212, 16, v213
	v_and_b32_e32 v213, 0xffff0000, v213
	v_pk_add_f32 v[164:165], v[164:165], v[212:213]
	v_lshlrev_b32_e32 v208, 16, v209
	v_and_b32_e32 v209, 0xffff0000, v209
	v_pk_add_f32 v[114:115], v[114:115], v[172:173]
	v_pk_add_f32 v[160:161], v[160:161], v[208:209]
	v_lshlrev_b32_e32 v198, 16, v199
	v_and_b32_e32 v199, 0xffff0000, v199
	v_pk_add_f32 v[156:157], v[156:157], v[198:199]
	v_lshlrev_b32_e32 v192, 16, v193
	v_and_b32_e32 v193, 0xffff0000, v193
	v_pk_add_f32 v[152:153], v[152:153], v[192:193]
	v_lshlrev_b32_e32 v184, 16, v185
	v_and_b32_e32 v185, 0xffff0000, v185
	v_pk_add_f32 v[126:127], v[126:127], v[184:185]
	v_lshlrev_b32_e32 v180, 16, v181
	v_and_b32_e32 v181, 0xffff0000, v181
	v_pk_add_f32 v[120:121], v[120:121], v[178:179]
	v_pk_add_f32 v[122:123], v[122:123], v[180:181]
	s_or_b32 s4, s3, s2
	s_cmp_eq_u32 s4, 0
	v_readfirstlane_b32 s5, v0
	v_readfirstlane_b32 s4, v0
	v_lshlrev_b32_e32 v170, 16, v226
	v_and_b32_e32 v171, 0xffff0000, v226
	v_pk_add_f32 v[166:167], v[166:167], v[170:171]
	v_lshlrev_b32_e32 v172, 16, v227
	v_and_b32_e32 v173, 0xffff0000, v227
	v_pk_add_f32 v[164:165], v[164:165], v[172:173]
	v_lshlrev_b32_e32 v170, 16, v232
	v_and_b32_e32 v171, 0xffff0000, v232
	v_pk_add_f32 v[162:163], v[162:163], v[170:171]
	v_lshlrev_b32_e32 v170, 16, v220
	v_and_b32_e32 v171, 0xffff0000, v220
	v_lshlrev_b32_e32 v172, 16, v233
	v_and_b32_e32 v173, 0xffff0000, v233
	v_pk_add_f32 v[158:159], v[158:159], v[170:171]
	v_lshlrev_b32_e32 v170, 16, v230
	v_and_b32_e32 v171, 0xffff0000, v230
	v_pk_add_f32 v[160:161], v[160:161], v[172:173]
	v_lshlrev_b32_e32 v172, 16, v221
	v_and_b32_e32 v173, 0xffff0000, v221
	v_pk_add_f32 v[154:155], v[154:155], v[170:171]
	v_lshlrev_b32_e32 v170, 16, v216
	v_and_b32_e32 v171, 0xffff0000, v216
	v_pk_add_f32 v[156:157], v[156:157], v[172:173]
	v_lshlrev_b32_e32 v172, 16, v231
	v_and_b32_e32 v173, 0xffff0000, v231
	v_pk_add_f32 v[146:147], v[146:147], v[170:171]
	v_lshlrev_b32_e32 v170, 16, v228
	v_and_b32_e32 v171, 0xffff0000, v228
	v_pk_add_f32 v[152:153], v[152:153], v[172:173]
	v_lshlrev_b32_e32 v172, 16, v217
	v_and_b32_e32 v173, 0xffff0000, v217
; __device__ __forceinline__ float bflo(unsigned w) { return __uint_as_float(w << 16); }
; __device__ __forceinline__ float bfhi(unsigned w) { return __uint_as_float(w & 0xffff0000u); }
; __device__ __forceinline__ int shl_from_i(int v, int src_lane) { return __builtin_amdgcn_ds_bpermute(src_lane << 2, v); }
; __device__ __forceinline__ void p1_gather_consume(f32x4 (&va)[4], f32x4 (&vb)[4], u32x2 (&wa)[4][4], u32x2 (&wb)[4][4], unsigned maska, unsigned maskb, int inva, int invb,
;                                                   const bf16_t* Yp, const bf16_t* zrow, const f32x4 (&g2)[4], int lane) {
;     ...
;         for (int q = 0; q < 4; ++q)
; #pragma unroll
;             for (int j = 0; j < 4; ++j) { aa[j] += (f32x4){bflo(wa[q][j].x), bfhi(wa[q][j].x), bflo(wa[q][j].y), bfhi(wa[q][j].y)};
;                 ab[j] += (f32x4){bflo(wb[q][j].x), bfhi(wb[q][j].x), bflo(wb[q][j].y), bfhi(wb[q][j].y)}; }
;         if (!(maska | maskb)) break;
;         const bf16_t* ypa[4]; const bf16_t* ypb[4];
; #pragma unroll
;         for (int q = 0; q < 4; ++q) {
;             if (maska) { const int e = __builtin_ctz(maska); maska &= maska - 1; ypa[q] = Yp + (size_t)shl_from_i(inva, e) * D; } else ypa[q] = zrow;
;             if (maskb) { const int e = __builtin_ctz(maskb); maskb &= maskb - 1; ypb[q] = Yp + (size_t)shl_from_i(invb, e) * D; } else ypb[q] = zrow; }
	v_pk_add_f32 v[124:125], v[124:125], v[170:171]
	v_lshlrev_b32_e32 v170, 16, v210
	v_and_b32_e32 v171, 0xffff0000, v210
	v_pk_add_f32 v[126:127], v[126:127], v[172:173]
	v_lshlrev_b32_e32 v172, 16, v229
	v_and_b32_e32 v173, 0xffff0000, v229
	v_pk_add_f32 v[120:121], v[120:121], v[170:171]
	v_lshlrev_b32_e32 v170, 16, v224
	v_and_b32_e32 v171, 0xffff0000, v224
	v_pk_add_f32 v[122:123], v[122:123], v[172:173]
	v_lshlrev_b32_e32 v172, 16, v211
	v_and_b32_e32 v173, 0xffff0000, v211
	v_pk_add_f32 v[114:115], v[114:115], v[170:171]
	v_lshlrev_b32_e32 v170, 16, v206
	v_and_b32_e32 v171, 0xffff0000, v206
	v_pk_add_f32 v[118:119], v[118:119], v[172:173]
	v_lshlrev_b32_e32 v172, 16, v225
	v_and_b32_e32 v173, 0xffff0000, v225
	v_pk_add_f32 v[166:167], v[166:167], v[170:171]
	v_lshlrev_b32_e32 v170, 16, v222
	v_and_b32_e32 v171, 0xffff0000, v222
	v_pk_add_f32 v[116:117], v[116:117], v[172:173]
	v_lshlrev_b32_e32 v172, 16, v207
	v_and_b32_e32 v173, 0xffff0000, v207
	v_pk_add_f32 v[162:163], v[162:163], v[170:171]
	v_lshlrev_b32_e32 v170, 16, v200
	v_and_b32_e32 v171, 0xffff0000, v200
	v_pk_add_f32 v[164:165], v[164:165], v[172:173]
	v_lshlrev_b32_e32 v172, 16, v223
	v_and_b32_e32 v173, 0xffff0000, v223
	v_pk_add_f32 v[158:159], v[158:159], v[170:171]
	v_lshlrev_b32_e32 v170, 16, v218
	v_and_b32_e32 v171, 0xffff0000, v218
	v_pk_add_f32 v[160:161], v[160:161], v[172:173]
	v_lshlrev_b32_e32 v172, 16, v201
	v_and_b32_e32 v173, 0xffff0000, v201
	v_pk_add_f32 v[154:155], v[154:155], v[170:171]
	v_lshlrev_b32_e32 v170, 16, v194
	v_and_b32_e32 v171, 0xffff0000, v194
	v_pk_add_f32 v[156:157], v[156:157], v[172:173]
	v_lshlrev_b32_e32 v172, 16, v219
	v_and_b32_e32 v173, 0xffff0000, v219
	v_pk_add_f32 v[146:147], v[146:147], v[170:171]
	v_lshlrev_b32_e32 v170, 16, v214
	v_and_b32_e32 v171, 0xffff0000, v214
	v_pk_add_f32 v[152:153], v[152:153], v[172:173]
	v_lshlrev_b32_e32 v172, 16, v195
	v_and_b32_e32 v173, 0xffff0000, v195
	v_pk_add_f32 v[124:125], v[124:125], v[170:171]
	v_lshlrev_b32_e32 v170, 16, v190
	v_and_b32_e32 v171, 0xffff0000, v190
	v_pk_add_f32 v[126:127], v[126:127], v[172:173]
	v_lshlrev_b32_e32 v172, 16, v215
	v_and_b32_e32 v173, 0xffff0000, v215
	v_pk_add_f32 v[120:121], v[120:121], v[170:171]
	v_lshlrev_b32_e32 v170, 16, v204
	v_and_b32_e32 v171, 0xffff0000, v204
	v_pk_add_f32 v[122:123], v[122:123], v[172:173]
	v_lshlrev_b32_e32 v172, 16, v191
	v_and_b32_e32 v173, 0xffff0000, v191
	v_pk_add_f32 v[114:115], v[114:115], v[170:171]
	v_lshlrev_b32_e32 v170, 16, v186
	v_and_b32_e32 v171, 0xffff0000, v186
	v_pk_add_f32 v[118:119], v[118:119], v[172:173]
	v_lshlrev_b32_e32 v172, 16, v205
	v_and_b32_e32 v173, 0xffff0000, v205
	v_pk_add_f32 v[166:167], v[166:167], v[170:171]
	v_lshlrev_b32_e32 v170, 16, v202
	v_and_b32_e32 v171, 0xffff0000, v202
	v_pk_add_f32 v[116:117], v[116:117], v[172:173]
	v_lshlrev_b32_e32 v172, 16, v187
	v_and_b32_e32 v173, 0xffff0000, v187
	v_pk_add_f32 v[162:163], v[162:163], v[170:171]
	v_lshlrev_b32_e32 v170, 16, v176
	v_and_b32_e32 v171, 0xffff0000, v176
	v_pk_add_f32 v[164:165], v[164:165], v[172:173]
	v_lshlrev_b32_e32 v172, 16, v203
	v_and_b32_e32 v173, 0xffff0000, v203
	v_pk_add_f32 v[158:159], v[158:159], v[170:171]
	v_lshlrev_b32_e32 v170, 16, v196
	v_and_b32_e32 v171, 0xffff0000, v196
	v_pk_add_f32 v[160:161], v[160:161], v[172:173]
	v_lshlrev_b32_e32 v172, 16, v177
	v_and_b32_e32 v173, 0xffff0000, v177
	v_pk_add_f32 v[154:155], v[154:155], v[170:171]
	v_lshlrev_b32_e32 v170, 16, v174
	v_and_b32_e32 v171, 0xffff0000, v174
	v_pk_add_f32 v[156:157], v[156:157], v[172:173]
	v_lshlrev_b32_e32 v172, 16, v197
	v_and_b32_e32 v173, 0xffff0000, v197
	v_pk_add_f32 v[146:147], v[146:147], v[170:171]
	v_lshlrev_b32_e32 v170, 16, v188
	v_and_b32_e32 v171, 0xffff0000, v188
	v_pk_add_f32 v[152:153], v[152:153], v[172:173]
	v_lshlrev_b32_e32 v172, 16, v175
	v_and_b32_e32 v173, 0xffff0000, v175
	v_pk_add_f32 v[124:125], v[124:125], v[170:171]
	v_lshlrev_b32_e32 v170, 16, v168
	v_and_b32_e32 v171, 0xffff0000, v168
	v_lshlrev_b32_e32 v168, 16, v169
	v_and_b32_e32 v169, 0xffff0000, v169
	v_pk_add_f32 v[126:127], v[126:127], v[172:173]
	v_lshlrev_b32_e32 v172, 16, v189
	v_and_b32_e32 v173, 0xffff0000, v189
	v_pk_add_f32 v[118:119], v[118:119], v[168:169]
	v_pk_add_f32 v[120:121], v[120:121], v[170:171]
	v_lshlrev_b32_e32 v168, 16, v182
	v_and_b32_e32 v169, 0xffff0000, v182
	v_lshlrev_b32_e32 v170, 16, v183
	v_and_b32_e32 v171, 0xffff0000, v183
	v_pk_add_f32 v[122:123], v[122:123], v[172:173]
	v_pk_add_f32 v[116:117], v[116:117], v[170:171]
	v_pk_add_f32 v[114:115], v[114:115], v[168:169]
	s_cbranch_scc1 .LBB0_184
	s_mov_b32 s4, 0
	s_cmp_eq_u32 s3, 0
	v_mov_b64_e32 v[170:171], s[54:55]
	s_mov_b32 s5, 0
	s_cbranch_scc1 .LBB0_188
	s_ff1_i32_b32 s5, s3
	s_lshl_b32 s5, s5, 2
	v_mov_b32_e32 v168, s5
	ds_bpermute_b32 v168, v168, v245
	s_add_i32 s5, s3, -1
	s_and_b32 s5, s5, s3
	s_waitcnt lgkmcnt(0)
	v_ashrrev_i32_e32 v169, 31, v168
	v_lshlrev_b64 v[168:169], 11, v[168:169]
	v_lshl_add_u64 v[170:171], s[52:53], 0, v[168:169]

; __device__ __forceinline__ void p1_norm1(const Frame& F, int layer, int probe_rerun) {
;     ...
;         float sa = 0.f, sb = 0.f;
; #pragma unroll
;         for (int j = 0; j < 4; ++j) { sa += va[j][0] * va[j][0] + va[j][1] * va[j][1] + va[j][2] * va[j][2] + va[j][3] * va[j][3];
;             sb += vb[j][0] * vb[j][0] + vb[j][1] * vb[j][1] + vb[j][2] * vb[j][2] + vb[j][3] * vb[j][3]; }
;         sa = wave_sum_dpp(sa); sb = wave_sum_dpp(sb);
;         float ma = 0.f, mb = 0.f;
;         { const float rsa = rsqrtf(sa * (1.f / D) + EPS), rsb = rsqrtf(sb * (1.f / D) + EPS);
; #pragma unroll
;           for (int j = 0; j < 4; ++j) {
;               const f32x4 ha = va[j] * rsa * W1[j] + S0[j], hb = vb[j] * rsb * W1[j] + S0[j];
;               ma = fmaxf(fmaxf(ma, fmaxf(fabsf(ha[0]), fabsf(ha[1]))), fmaxf(fabsf(ha[2]), fabsf(ha[3])));
;               mb = fmaxf(fmaxf(mb, fmaxf(fabsf(hb[0]), fabsf(hb[1]))), fmaxf(fabsf(hb[2]), fabsf(hb[3])));
;               va[j] = ha; vb[j] = hb; } }
;         ma = wave_max_dpp(ma); mb = wave_max_dpp(mb);
.LBB0_205:
	v_mov_b32_e32 v114, v89
	v_mov_b32_e32 v115, v93
	v_mov_b32_e32 v112, v88
	v_mov_b32_e32 v113, v92
	v_pk_mul_f32 v[114:115], v[114:115], v[114:115]
	v_mov_b32_e32 v116, v105
	v_pk_fma_f32 v[112:113], v[112:113], v[112:113], v[114:115]
	v_mov_b32_e32 v114, v90
	v_mov_b32_e32 v115, v94
	v_pk_fma_f32 v[112:113], v[114:115], v[114:115], v[112:113]
	v_mov_b32_e32 v114, v91
	v_mov_b32_e32 v115, v95
	v_mov_b32_e32 v117, v109
	v_pk_fma_f32 v[112:113], v[114:115], v[114:115], v[112:113]
	v_mov_b32_e32 v114, v104
	v_mov_b32_e32 v115, v108
	v_pk_mul_f32 v[116:117], v[116:117], v[116:117]
	v_mov_b32_e32 v118, v81
	v_pk_fma_f32 v[114:115], v[114:115], v[114:115], v[116:117]
	v_mov_b32_e32 v116, v106
	v_mov_b32_e32 v117, v110
	v_pk_fma_f32 v[114:115], v[116:117], v[116:117], v[114:115]
	v_mov_b32_e32 v116, v107
	v_mov_b32_e32 v117, v111
	v_mov_b32_e32 v119, v85
	v_pk_fma_f32 v[114:115], v[116:117], v[116:117], v[114:115]
	v_mov_b32_e32 v116, v80
	v_mov_b32_e32 v117, v84
	v_pk_mul_f32 v[118:119], v[118:119], v[118:119]
	v_add_f32_e32 v112, v112, v113
	v_pk_fma_f32 v[116:117], v[116:117], v[116:117], v[118:119]
	v_mov_b32_e32 v118, v82
	v_mov_b32_e32 v119, v86
	v_pk_fma_f32 v[116:117], v[118:119], v[118:119], v[116:117]
	v_mov_b32_e32 v118, v83
	v_mov_b32_e32 v119, v87
	v_pk_fma_f32 v[116:117], v[118:119], v[118:119], v[116:117]
	v_mov_b32_e32 v113, v100
	v_add_f32_e32 v112, v117, v112
	v_add_f32_e32 v118, v116, v112
	v_mov_b32_e32 v116, v97
	v_mov_b32_e32 v117, v101
	v_mov_b32_e32 v112, v96
	v_pk_mul_f32 v[116:117], v[116:117], v[116:117]
	v_add_f32_e32 v114, v114, v115
	v_pk_fma_f32 v[112:113], v[112:113], v[112:113], v[116:117]
	v_mov_b32_e32 v116, v98
	v_mov_b32_e32 v117, v102
	v_pk_fma_f32 v[112:113], v[116:117], v[116:117], v[112:113]
	v_mov_b32_e32 v116, v99
	v_mov_b32_e32 v117, v103
	v_pk_fma_f32 v[112:113], v[116:117], v[116:117], v[112:113]
	s_nop 0
	v_add_f32_e32 v113, v113, v114
	v_add_f32_e32 v114, v112, v113
	v_add_f32_dpp v112, v118, v118 quad_perm:[1,0,3,2] row_mask:0xf bank_mask:0xf bound_ctrl:1
	s_nop 0
	v_add_f32_dpp v114, v114, v114 quad_perm:[1,0,3,2] row_mask:0xf bank_mask:0xf bound_ctrl:1
	v_add_f32_dpp v112, v112, v112 quad_perm:[2,3,0,1] row_mask:0xf bank_mask:0xf bound_ctrl:1
	s_nop 0
	v_add_f32_dpp v114, v114, v114 quad_perm:[2,3,0,1] row_mask:0xf bank_mask:0xf bound_ctrl:1
	v_add_f32_dpp v112, v112, v112 row_half_mirror row_mask:0xf bank_mask:0xf bound_ctrl:1
	s_nop 0
	v_add_f32_dpp v114, v114, v114 row_half_mirror row_mask:0xf bank_mask:0xf bound_ctrl:1
	v_add_f32_dpp v112, v112, v112 row_mirror row_mask:0xf bank_mask:0xf bound_ctrl:1
	s_nop 0
	v_readlane_b32 s4, v112, 16
	v_readlane_b32 s5, v112, 48
	v_add_f32_dpp v114, v114, v114 row_mirror row_mask:0xf bank_mask:0xf bound_ctrl:1
	v_readlane_b32 s2, v112, 0
	v_readlane_b32 s3, v112, 32
	v_mov_b32_e32 v112, s4
	v_mov_b32_e32 v113, s5
	v_readlane_b32 s4, v114, 16
	v_readlane_b32 s5, v114, 48
	v_pk_add_f32 v[112:113], s[2:3], v[112:113]
	v_readlane_b32 s2, v114, 0
	v_readlane_b32 s3, v114, 32
	v_mov_b32_e32 v114, s4
	v_mov_b32_e32 v115, s5
	v_pk_add_f32 v[114:115], s[2:3], v[114:115]
	v_mov_b32_e32 v117, v112
	v_mov_b32_e32 v116, v114
	v_mov_b32_e32 v112, v115
	v_pk_add_f32 v[112:113], v[116:117], v[112:113]
	s_nop 0
	v_pk_fma_f32 v[112:113], v[112:113], s[86:87], v[246:247] op_sel_hi:[1,0,0]
	s_nop 0
	v_mul_f32_e32 v114, 0x4b800000, v113
	v_cmp_gt_f32_e32 vcc, s22, v113
	v_cmp_gt_f32_e64 s[40:41], s22, v112
	s_nop 0
	v_cndmask_b32_e32 v113, v113, v114, vcc
	v_mul_f32_e32 v114, 0x4b800000, v112
	v_rsq_f32_e32 v113, v113
	v_cndmask_b32_e64 v112, v112, v114, s[40:41]
	v_rsq_f32_e32 v112, v112
	v_mul_f32_e32 v114, 0x45800000, v113
	v_cndmask_b32_e32 v116, v113, v114, vcc
	v_mul_f32_e32 v113, 0x45800000, v112
	v_cndmask_b32_e64 v118, v112, v113, s[40:41]
	v_pk_mul_f32 v[92:93], v[116:117], v[92:93] op_sel_hi:[0,1]
	v_pk_mul_f32 v[94:95], v[116:117], v[94:95] op_sel_hi:[0,1]
	v_pk_fma_f32 v[112:113], v[74:75], v[94:95], v[50:51]
	v_pk_fma_f32 v[114:115], v[72:73], v[92:93], v[48:49]
	v_pk_mul_f32 v[94:95], v[118:119], v[108:109] op_sel_hi:[0,1]
	v_pk_mul_f32 v[92:93], v[118:119], v[110:111] op_sel_hi:[0,1]
	v_pk_fma_f32 v[92:93], v[74:75], v[92:93], v[50:51]
	v_pk_fma_f32 v[94:95], v[72:73], v[94:95], v[48:49]
	v_max_f32_e64 v108, |v114|, |v115|
	v_max_f32_e64 v109, |v112|, |v113|
	v_max3_f32 v117, v108, 0, v109
	v_max_f32_e64 v108, |v94|, |v95|
	v_max_f32_e64 v109, |v92|, |v93|
	v_max3_f32 v119, v108, 0, v109
	v_pk_mul_f32 v[88:89], v[116:117], v[88:89] op_sel_hi:[0,1]
	v_pk_mul_f32 v[90:91], v[116:117], v[90:91] op_sel_hi:[0,1]
	v_pk_fma_f32 v[108:109], v[70:71], v[90:91], v[54:55]
	v_pk_fma_f32 v[110:111], v[68:69], v[88:89], v[52:53]
	v_pk_mul_f32 v[90:91], v[118:119], v[104:105] op_sel_hi:[0,1]
	v_pk_mul_f32 v[88:89], v[118:119], v[106:107] op_sel_hi:[0,1]
	v_pk_fma_f32 v[88:89], v[70:71], v[88:89], v[54:55]
	v_pk_fma_f32 v[90:91], v[68:69], v[90:91], v[52:53]
	v_max_f32_e64 v104, |v110|, |v111|
	v_max_f32_e64 v105, |v108|, |v109|
	v_max3_f32 v117, v117, v104, v105
	v_max_f32_e64 v104, |v90|, |v91|
	v_max_f32_e64 v105, |v88|, |v89|
	v_max3_f32 v119, v119, v104, v105
	v_pk_mul_f32 v[84:85], v[116:117], v[84:85] op_sel_hi:[0,1]
	v_pk_mul_f32 v[86:87], v[116:117], v[86:87] op_sel_hi:[0,1]
	v_pk_fma_f32 v[104:105], v[66:67], v[86:87], v[58:59]
	v_pk_fma_f32 v[106:107], v[64:65], v[84:85], v[56:57]
	v_pk_mul_f32 v[86:87], v[118:119], v[100:101] op_sel_hi:[0,1]
	v_pk_mul_f32 v[84:85], v[118:119], v[102:103] op_sel_hi:[0,1]
	v_pk_fma_f32 v[84:85], v[66:67], v[84:85], v[58:59]
	v_pk_fma_f32 v[86:87], v[64:65], v[86:87], v[56:57]
	v_max_f32_e64 v100, |v106|, |v107|
; __device__ __forceinline__ void p1_norm1(const Frame& F, int layer, int probe_rerun) {
;     ...
;           for (int j = 0; j < 4; ++j) {
;               const f32x4 ha = va[j] * rsa * W1[j] + S0[j], hb = vb[j] * rsb * W1[j] + S0[j];
;               ma = fmaxf(fmaxf(ma, fmaxf(fabsf(ha[0]), fabsf(ha[1]))), fmaxf(fabsf(ha[2]), fabsf(ha[3])));
;               mb = fmaxf(fmaxf(mb, fmaxf(fabsf(hb[0]), fabsf(hb[1]))), fmaxf(fabsf(hb[2]), fabsf(hb[3])));
;               va[j] = ha; vb[j] = hb; } }
;         ma = wave_max_dpp(ma); mb = wave_max_dpp(mb);
;         if (vR) { const float ia = ma > 0.f ? 127.f / ma : 0.f, ib = mb > 0.f ? 127.f / mb : 0.f;
; #pragma unroll
;           for (int j = 0; j < 4; ++j) { const int k = 4 * (lane + 64 * j);
;               const unsigned qa = pack_i8x4(va[j][0], va[j][1], va[j][2], va[j][3], ia), qb = pack_i8x4(vb[j][0], vb[j][1], vb[j][2], vb[j][3], ib);
;               *(unsigned*)(HQp + (size_t)rowA * D + k) = qa; *(unsigned*)(HQp + (size_t)rowB * D + k) = qb; }
;           if (lane == 0) { SAp[rowA] = ma * (1.f / 127.f); SAp[rowB] = mb * (1.f / 127.f); } }
	v_max_f32_e64 v101, |v104|, |v105|
	v_max3_f32 v117, v117, v100, v101
	v_max_f32_e64 v100, |v86|, |v87|
	v_max_f32_e64 v101, |v84|, |v85|
	v_max3_f32 v119, v119, v100, v101
	v_pk_mul_f32 v[80:81], v[116:117], v[80:81] op_sel_hi:[0,1]
	v_pk_mul_f32 v[82:83], v[116:117], v[82:83] op_sel_hi:[0,1]
	v_pk_fma_f32 v[100:101], v[78:79], v[82:83], v[62:63]
	v_pk_fma_f32 v[102:103], v[76:77], v[80:81], v[60:61]
	v_pk_mul_f32 v[82:83], v[118:119], v[96:97] op_sel_hi:[0,1]
	v_pk_mul_f32 v[80:81], v[118:119], v[98:99] op_sel_hi:[0,1]
	v_pk_fma_f32 v[80:81], v[78:79], v[80:81], v[62:63]
	v_pk_fma_f32 v[82:83], v[76:77], v[82:83], v[60:61]
	v_max_f32_e64 v96, |v102|, |v103|
	v_max_f32_e64 v97, |v100|, |v101|
	v_max3_f32 v96, v117, v96, v97
	v_max_f32_e64 v97, |v82|, |v83|
	v_max_f32_e64 v98, |v80|, |v81|
	v_max3_f32 v97, v119, v97, v98
	s_andn2_b64 vcc, exec, s[60:61]
	v_mov_b32_dpp v98, v96 quad_perm:[1,0,3,2] row_mask:0xf bank_mask:0xf bound_ctrl:1
	v_max_f32_e32 v98, v98, v98
	v_max_f32_e32 v96, v96, v98
	s_nop 1
	v_mov_b32_dpp v98, v96 quad_perm:[2,3,0,1] row_mask:0xf bank_mask:0xf bound_ctrl:1
	v_max_f32_e32 v98, v98, v98
	v_max_f32_e32 v96, v96, v98
	s_nop 1
	v_mov_b32_dpp v98, v96 row_half_mirror row_mask:0xf bank_mask:0xf bound_ctrl:1
	v_max_f32_e32 v98, v98, v98
	v_max_f32_e32 v96, v96, v98
	s_nop 1
	v_mov_b32_dpp v98, v96 row_mirror row_mask:0xf bank_mask:0xf bound_ctrl:1
	v_max_f32_e32 v98, v98, v98
	v_max_f32_e32 v96, v96, v98
	s_nop 0
	v_readlane_b32 s2, v96, 0
	v_readlane_b32 s3, v96, 16
	v_readlane_b32 s4, v96, 32
	v_readlane_b32 s5, v96, 48
	v_mov_b32_dpp v96, v97 quad_perm:[1,0,3,2] row_mask:0xf bank_mask:0xf bound_ctrl:1
	v_max_f32_e32 v96, v96, v96
	v_max_f32_e32 v96, v97, v96
	s_nop 1
	v_mov_b32_dpp v97, v96 quad_perm:[2,3,0,1] row_mask:0xf bank_mask:0xf bound_ctrl:1
	v_max_f32_e32 v97, v97, v97
	v_max_f32_e32 v96, v96, v97
	s_nop 1
	v_mov_b32_dpp v97, v96 row_half_mirror row_mask:0xf bank_mask:0xf bound_ctrl:1
	v_max_f32_e32 v97, v97, v97
	v_max_f32_e32 v96, v96, v97
	s_nop 1
	v_mov_b32_dpp v97, v96 row_mirror row_mask:0xf bank_mask:0xf bound_ctrl:1
	v_max_f32_e32 v97, v97, v97
	v_max_f32_e32 v96, v96, v97
	s_nop 0
	v_readlane_b32 s6, v96, 0
	v_readlane_b32 s7, v96, 16
	v_readlane_b32 s28, v96, 32
	v_readlane_b32 s29, v96, 48
	s_cbranch_vccnz .LBB0_209
	v_max_f32_e64 v96, s5, s5
	v_max_f32_e64 v99, s4, s4
	v_max_f32_e32 v96, v99, v96
	v_mov_b32_e32 v99, s3
	v_max3_f32 v96, s2, v99, v96
	s_mov_b32 s4, 0x42fe0000
	v_div_scale_f32 v99, s[2:3], v96, v96, s4
	v_rcp_f32_e32 v116, v99
	v_max_f32_e64 v97, s29, s29
	v_max_f32_e64 v98, s28, s28
	v_max_f32_e32 v97, v98, v97
	v_mov_b32_e32 v98, s7
	v_max3_f32 v97, s6, v98, v97
	v_fma_f32 v98, -v99, v116, 1.0
	v_fmac_f32_e32 v116, v98, v116
	v_div_scale_f32 v98, vcc, s4, v96, s4
	v_mul_f32_e32 v117, v98, v116
	v_fma_f32 v118, -v99, v117, v98
	v_fmac_f32_e32 v117, v118, v116
	v_fma_f32 v98, -v99, v117, v98
	v_div_scale_f32 v99, s[2:3], v97, v97, s4
	v_div_fmas_f32 v98, v98, v116, v117
	v_rcp_f32_e32 v116, v99
	v_div_fixup_f32 v98, v98, v96, s4
	v_cmp_lt_f32_e32 vcc, 0, v96
	s_mov_b32 s6, 0xc0c0400
	s_mov_b32 s7, 0x5040100
	v_cndmask_b32_e32 v118, 0, v98, vcc
	v_fma_f32 v98, -v99, v116, 1.0
	v_fmac_f32_e32 v116, v98, v116
	v_div_scale_f32 v98, vcc, s4, v97, s4
	v_mul_f32_e32 v117, v98, v116
	v_fma_f32 v119, -v99, v117, v98
	v_fmac_f32_e32 v117, v119, v116
	v_fma_f32 v98, -v99, v117, v98
	v_div_fmas_f32 v98, v98, v116, v117
	v_div_fixup_f32 v98, v98, v97, s4
	v_cmp_lt_f32_e32 vcc, 0, v97
	v_fmaak_f32 v99, v115, v118, 0x4b400000
	v_fmaak_f32 v116, v112, v118, 0x4b400000
	v_cndmask_b32_e32 v119, 0, v98, vcc
	v_fmaak_f32 v98, v114, v118, 0x4b400000
	v_fmaak_f32 v117, v113, v118, 0x4b400000
	v_perm_b32 v98, v99, v98, s6
	v_perm_b32 v99, v117, v116, s6
	s_ashr_i32 s59, s58, 31
	v_perm_b32 v116, v99, v98, s7
	v_fmaak_f32 v98, v94, v119, 0x4b400000
	v_fmaak_f32 v99, v95, v119, 0x4b400000
	v_fmaak_f32 v117, v92, v119, 0x4b400000
	v_fmaak_f32 v120, v93, v119, 0x4b400000
	s_lshl_b64 s[2:3], s[58:59], 10
	s_ashr_i32 s63, s62, 31
	v_perm_b32 v98, v99, v98, s6
	v_perm_b32 v99, v120, v117, s6
	s_lshl_b64 s[4:5], s[62:63], 10
	v_perm_b32 v120, v99, v98, s7
	v_lshl_add_u64 v[98:99], v[150:151], 0, s[2:3]
	global_store_dword v[98:99], v116, off
	v_lshl_add_u64 v[116:117], v[150:151], 0, s[4:5]
	global_store_dword v[116:117], v120, off
	v_fmaak_f32 v120, v110, v118, 0x4b400000
	v_fmaak_f32 v121, v111, v118, 0x4b400000
	v_fmaak_f32 v122, v108, v118, 0x4b400000
	v_fmaak_f32 v123, v109, v118, 0x4b400000
	v_perm_b32 v120, v121, v120, s6
	v_perm_b32 v121, v123, v122, s6
	v_perm_b32 v120, v121, v120, s7
	v_fmaak_f32 v121, v90, v119, 0x4b400000
	v_fmaak_f32 v122, v91, v119, 0x4b400000
	v_fmaak_f32 v123, v88, v119, 0x4b400000
	v_fmaak_f32 v124, v89, v119, 0x4b400000
	v_perm_b32 v121, v122, v121, s6
	v_perm_b32 v122, v124, v123, s6
	v_perm_b32 v121, v122, v121, s7
	global_store_dword v[98:99], v120, off offset:256
	global_store_dword v[116:117], v121, off offset:256
	v_fmaak_f32 v120, v106, v118, 0x4b400000
	v_fmaak_f32 v121, v107, v118, 0x4b400000
	v_fmaak_f32 v122, v104, v118, 0x4b400000
	v_fmaak_f32 v123, v105, v118, 0x4b400000
	v_perm_b32 v120, v121, v120, s6
	v_perm_b32 v121, v123, v122, s6
	v_perm_b32 v120, v121, v120, s7
	v_fmaak_f32 v121, v86, v119, 0x4b400000
	v_fmaak_f32 v122, v87, v119, 0x4b400000
	v_fmaak_f32 v123, v84, v119, 0x4b400000
	v_fmaak_f32 v124, v85, v119, 0x4b400000
	v_perm_b32 v121, v122, v121, s6
	v_perm_b32 v122, v124, v123, s6
	v_perm_b32 v121, v122, v121, s7
	global_store_dword v[98:99], v120, off offset:512
	global_store_dword v[116:117], v121, off offset:512
	v_fmaak_f32 v120, v102, v118, 0x4b400000
	v_fmaak_f32 v121, v103, v118, 0x4b400000
	v_fmaak_f32 v122, v100, v118, 0x4b400000
	v_fmaak_f32 v118, v101, v118, 0x4b400000
	v_perm_b32 v120, v121, v120, s6
	v_perm_b32 v118, v118, v122, s6
	v_perm_b32 v118, v118, v120, s7
	v_fmaak_f32 v120, v82, v119, 0x4b400000
	v_fmaak_f32 v121, v83, v119, 0x4b400000
	v_fmaak_f32 v122, v80, v119, 0x4b400000
	v_fmaak_f32 v119, v81, v119, 0x4b400000
	v_perm_b32 v120, v121, v120, s6
	v_perm_b32 v119, v119, v122, s6
	v_perm_b32 v119, v119, v120, s7
	global_store_dword v[98:99], v118, off offset:768
	global_store_dword v[116:117], v119, off offset:768
	s_and_saveexec_b64 s[2:3], s[38:39]
	s_cbranch_execz .LBB0_208
	s_lshl_b64 s[4:5], s[58:59], 2
	s_add_u32 s4, s12, s4
	s_addc_u32 s5, s13, s5
	s_lshl_b64 s[6:7], s[62:63], 2
	v_mul_f32_e32 v96, 0x3c010204, v96
	s_add_u32 s6, s12, s6
	v_mul_f32_e32 v97, 0x3c010204, v97
	s_addc_u32 s7, s13, s7
	global_store_dword v145, v96, s[4:5]
	global_store_dword v145, v97, s[6:7]

; #define LAS __attribute__((address_space(3)))
; __device__ __forceinline__ unsigned pk2(float lo, float hi) { f32x2_t v = {lo, hi}; bf16x2_t b = __builtin_convertvector(v, bf16x2_t); return __builtin_bit_cast(unsigned, b); }
; __device__ __forceinline__ float bflo(unsigned w) { return __uint_as_float(w << 16); }
; __device__ __forceinline__ float bfhi(unsigned w) { return __uint_as_float(w & 0xffff0000u); }
; __device__ __forceinline__ int shl_from_i(int v, int src_lane) { return __builtin_amdgcn_ds_bpermute(src_lane << 2, v); }
; __device__ __forceinline__ void thin_stage_row(LAS unsigned char* L, int srow, const f32x4 (&h)[4], int lane) {
; #pragma unroll
;     for (int j = 0; j < 4; ++j) { const int k = 4 * (lane + 64 * j);
;         const u32x2 hi = {pk2(h[j][0], h[j][1]), pk2(h[j][2], h[j][3])};
;         const u32x2 lo = {pk2(h[j][0] - bflo(hi.x), h[j][1] - bfhi(hi.x)), pk2(h[j][2] - bflo(hi.y), h[j][3] - bfhi(hi.y))};
;         *(LAS u32x2*)(L + TH_HHI + srow * TH_STR + k * 2) = hi; *(LAS u32x2*)(L + TH_HLO + srow * TH_STR + k * 2) = lo; }
; }
; __device__ __forceinline__ void p1_gather_issue(u32x2 (&wa)[4][4], u32x2 (&wb)[4][4], unsigned& maska, unsigned& maskb, int inva, int invb, const bf16_t* Yp, const bf16_t* zrow, int lane) {
;     maska = (unsigned)__ballot(inva >= 0) & 0xffffu; maskb = (unsigned)__ballot(invb >= 0) & 0xffffu;
;     const bf16_t* ypa[4]; const bf16_t* ypb[4];
; #pragma unroll
;     for (int q = 0; q < 4; ++q) {
;         if (maska) { const int e = __builtin_ctz(maska); maska &= maska - 1; ypa[q] = Yp + (size_t)shl_from_i(inva, e) * D; } else ypa[q] = zrow;
;         if (maskb) { const int e = __builtin_ctz(maskb); maskb &= maskb - 1; ypb[q] = Yp + (size_t)shl_from_i(invb, e) * D; } else ypb[q] = zrow; }
.LBB0_209:
	v_cvt_pk_bf16_f32 v96, v114, v115
	v_cvt_pk_bf16_f32 v97, v112, v113
	v_lshlrev_b32_e32 v98, 16, v96
	v_and_b32_e32 v99, 0xffff0000, v96
	v_pk_add_f32 v[98:99], v[114:115], v[98:99] neg_lo:[0,1] neg_hi:[0,1]
	v_lshlrev_b32_e32 v114, 16, v97
	v_and_b32_e32 v115, 0xffff0000, v97
	v_pk_add_f32 v[112:113], v[112:113], v[114:115] neg_lo:[0,1] neg_hi:[0,1]
	v_cvt_pk_bf16_f32 v98, v98, v99
	v_cvt_pk_bf16_f32 v99, v112, v113
	v_cvt_pk_bf16_f32 v112, v110, v111
	v_cvt_pk_bf16_f32 v113, v108, v109
	v_lshlrev_b32_e32 v114, 16, v112
	v_and_b32_e32 v115, 0xffff0000, v112
	v_pk_add_f32 v[110:111], v[110:111], v[114:115] neg_lo:[0,1] neg_hi:[0,1]
	v_lshlrev_b32_e32 v114, 16, v113
	v_and_b32_e32 v115, 0xffff0000, v113
	v_add_u32_e32 v116, s17, v236
	v_pk_add_f32 v[108:109], v[108:109], v[114:115] neg_lo:[0,1] neg_hi:[0,1]
	v_add_u32_e32 v117, s18, v236
	v_cvt_pk_bf16_f32 v110, v110, v111
	v_cvt_pk_bf16_f32 v111, v108, v109
	ds_write2st64_b64 v116, v[96:97], v[112:113] offset1:1
	ds_write2st64_b64 v117, v[98:99], v[110:111] offset1:1
	v_cvt_pk_bf16_f32 v96, v106, v107
	v_cvt_pk_bf16_f32 v97, v104, v105
	v_lshlrev_b32_e32 v98, 16, v96
	v_and_b32_e32 v99, 0xffff0000, v96
	v_pk_add_f32 v[98:99], v[106:107], v[98:99] neg_lo:[0,1] neg_hi:[0,1]
	v_lshlrev_b32_e32 v106, 16, v97
	v_and_b32_e32 v107, 0xffff0000, v97
	v_pk_add_f32 v[104:105], v[104:105], v[106:107] neg_lo:[0,1] neg_hi:[0,1]
	v_cvt_pk_bf16_f32 v98, v98, v99
	v_cvt_pk_bf16_f32 v99, v104, v105
	v_cvt_pk_bf16_f32 v104, v102, v103
	v_cvt_pk_bf16_f32 v105, v100, v101
	v_lshlrev_b32_e32 v106, 16, v104
	v_and_b32_e32 v107, 0xffff0000, v104
	v_pk_add_f32 v[102:103], v[102:103], v[106:107] neg_lo:[0,1] neg_hi:[0,1]
	v_lshlrev_b32_e32 v106, 16, v105
	v_and_b32_e32 v107, 0xffff0000, v105
	v_pk_add_f32 v[100:101], v[100:101], v[106:107] neg_lo:[0,1] neg_hi:[0,1]
	v_cvt_pk_bf16_f32 v102, v102, v103
	v_cvt_pk_bf16_f32 v103, v100, v101
	ds_write2st64_b64 v116, v[96:97], v[104:105] offset0:2 offset1:3
	ds_write2st64_b64 v117, v[98:99], v[102:103] offset0:2 offset1:3
	v_cvt_pk_bf16_f32 v96, v94, v95
	v_cvt_pk_bf16_f32 v97, v92, v93
	v_lshlrev_b32_e32 v98, 16, v96
	v_and_b32_e32 v99, 0xffff0000, v96
	v_pk_add_f32 v[94:95], v[94:95], v[98:99] neg_lo:[0,1] neg_hi:[0,1]
	v_lshlrev_b32_e32 v98, 16, v97
	v_and_b32_e32 v99, 0xffff0000, v97
	v_pk_add_f32 v[92:93], v[92:93], v[98:99] neg_lo:[0,1] neg_hi:[0,1]
	v_cvt_pk_bf16_f32 v94, v94, v95
	v_cvt_pk_bf16_f32 v95, v92, v93
	v_cvt_pk_bf16_f32 v92, v90, v91
	ds_write_b64 v239, v[96:97]
	ds_write_b64 v240, v[94:95]
	v_cvt_pk_bf16_f32 v93, v88, v89
	v_lshlrev_b32_e32 v94, 16, v92
	v_and_b32_e32 v95, 0xffff0000, v92
	v_pk_add_f32 v[90:91], v[90:91], v[94:95] neg_lo:[0,1] neg_hi:[0,1]
	v_lshlrev_b32_e32 v94, 16, v93
	v_and_b32_e32 v95, 0xffff0000, v93
	v_pk_add_f32 v[88:89], v[88:89], v[94:95] neg_lo:[0,1] neg_hi:[0,1]
	v_cvt_pk_bf16_f32 v90, v90, v91
	v_cvt_pk_bf16_f32 v91, v88, v89
	v_cvt_pk_bf16_f32 v88, v86, v87
	v_cvt_pk_bf16_f32 v89, v84, v85
	v_lshlrev_b32_e32 v94, 16, v88
	v_and_b32_e32 v95, 0xffff0000, v88
	v_pk_add_f32 v[86:87], v[86:87], v[94:95] neg_lo:[0,1] neg_hi:[0,1]
	v_lshlrev_b32_e32 v94, 16, v89
	v_and_b32_e32 v95, 0xffff0000, v89
	v_pk_add_f32 v[84:85], v[84:85], v[94:95] neg_lo:[0,1] neg_hi:[0,1]
	v_add_u32_e32 v96, s19, v236
	v_cvt_pk_bf16_f32 v86, v86, v87
	v_cvt_pk_bf16_f32 v87, v84, v85
	v_cvt_pk_bf16_f32 v84, v82, v83
	v_add_u32_e32 v97, s20, v236
	ds_write2st64_b64 v96, v[92:93], v[88:89] offset0:1 offset1:2
	ds_write2st64_b64 v97, v[90:91], v[86:87] offset0:1 offset1:2
	v_cvt_pk_bf16_f32 v85, v80, v81
	v_lshlrev_b32_e32 v86, 16, v84
	v_and_b32_e32 v87, 0xffff0000, v84
	v_pk_add_f32 v[82:83], v[82:83], v[86:87] neg_lo:[0,1] neg_hi:[0,1]
	v_lshlrev_b32_e32 v86, 16, v85
	v_and_b32_e32 v87, 0xffff0000, v85
	v_pk_add_f32 v[80:81], v[80:81], v[86:87] neg_lo:[0,1] neg_hi:[0,1]
	v_cvt_pk_bf16_f32 v82, v82, v83
	v_cvt_pk_bf16_f32 v83, v80, v81
	ds_write_b64 v96, v[84:85] offset:1536
	ds_write_b64 v97, v[82:83] offset:1536
	s_cmp_eq_u64 s[48:49], 0
	s_cbranch_scc1 .Lp1pf_skip
	s_cmp_ge_i32 s16, s64
	s_cbranch_scc1 .Lp1pf_skip
	s_waitcnt vmcnt(0)
	v_cmp_lt_i32_e64 s[68:69], -1, v243
	v_cmp_lt_i32_e64 s[70:71], -1, v144
	s_and_b32 s72, s68, 0xffff
	s_and_b32 s76, s70, 0xffff
	s_ff1_i32_b32 s90, s72
	s_add_i32 s73, s72, -1
	s_and_b32 s73, s73, s72
	s_lshl_b32 s90, s90, 2
	s_ff1_i32_b32 s91, s73
	s_add_i32 s74, s73, -1
	s_and_b32 s74, s74, s73
	s_lshl_b32 s91, s91, 2
	s_ff1_i32_b32 s92, s74
	s_add_i32 s75, s74, -1
	s_and_b32 s75, s75, s74
	s_lshl_b32 s92, s92, 2
	s_ff1_i32_b32 s93, s75
	s_add_i32 s99, s75, -1
	s_and_b32 s99, s99, s75
	s_lshl_b32 s93, s93, 2
	s_ff1_i32_b32 s94, s76
	s_add_i32 s67, s76, -1
	s_and_b32 s67, s67, s76
	s_lshl_b32 s94, s94, 2
	s_ff1_i32_b32 s95, s67
	s_add_i32 s88, s67, -1
	s_and_b32 s88, s88, s67
	s_lshl_b32 s95, s95, 2
	s_ff1_i32_b32 s96, s88
	s_add_i32 s89, s88, -1
	s_and_b32 s89, s89, s88
	s_lshl_b32 s96, s96, 2
	s_ff1_i32_b32 s68, s89
	s_add_i32 s98, s89, -1
	s_and_b32 s98, s98, s89
	s_lshl_b32 s68, s68, 2
	v_mov_b32_e32 v112, s90
	ds_bpermute_b32 v114, v112, v243
	v_mov_b32_e32 v113, s94
	ds_bpermute_b32 v116, v113, v144
	v_mov_b32_e32 v112, s91
	ds_bpermute_b32 v174, v112, v243
	v_mov_b32_e32 v113, s95
	ds_bpermute_b32 v168, v113, v144
	v_mov_b32_e32 v112, s92
	ds_bpermute_b32 v176, v112, v243
	v_mov_b32_e32 v113, s96
	ds_bpermute_b32 v182, v113, v144
	v_mov_b32_e32 v112, s93
	ds_bpermute_b32 v186, v112, v243
	v_mov_b32_e32 v113, s68
	ds_bpermute_b32 v188, v113, v144
	s_waitcnt lgkmcnt(0)
	s_cmp_eq_u32 s72, 0
	s_cbranch_scc1 .Lp1pf_e0
	v_ashrrev_i32_e32 v115, 31, v114
	v_lshlrev_b64 v[114:115], 11, v[114:115]
	v_lshl_add_u64 v[114:115], s[52:53], 0, v[114:115]
	s_branch .Lp1pf_n0
